# v48 + MoBA routing k_mean staging: the 16 per-thread k_mean loads issued together instead of one load and one full wait per loop trip
# speedup vs baseline: 1.0212x; 1.0018x over previous
.LBB0_818:
	s_cmp_lt_u32 s38, 4
	s_cbranch_scc1 .LBB0_817
	s_ashr_i32 s39, s38, 2
	s_and_b32 s49, s38, 3
	s_and_b32 s12, s37, 3
	v_lshl_add_u32 v58, s39, 8, v1
	s_lshl_b32 s18, s49, 22
	s_add_u32 s18, s46, s18
	v_ashrrev_i32_e32 v59, 31, v58
	s_addc_u32 s19, s47, 0
	s_waitcnt lgkmcnt(0)
	v_lshlrev_b64 v[2:3], 8, v[58:59]
	v_lshl_add_u64 v[2:3], s[18:19], 0, v[2:3]
	v_mov_b32_e32 v57, v51
	v_lshl_add_u64 v[2:3], v[2:3], 0, v[56:57]
	v_lshl_add_u64 v[4:5], v[2:3], 0, s[14:15]
	v_add_co_u32_e32 v2, vcc, 0x9000000, v2
	v_lshl_or_b32 v50, s12, 15, v66
	s_nop 0
	v_addc_co_u32_e32 v3, vcc, 0, v3, vcc
	global_load_dwordx4 v[18:21], v[4:5], off offset:32
	global_load_dwordx4 v[22:25], v[4:5], off offset:64
	global_load_dwordx4 v[26:29], v[4:5], off offset:96
	global_load_dwordx4 v[30:33], v[4:5], off offset:128
	global_load_dwordx4 v[34:37], v[4:5], off offset:160
	global_load_dwordx4 v[38:41], v[4:5], off offset:192
	global_load_dwordx4 v[42:45], v[2:3], off
	global_load_dwordx4 v[46:49], v[4:5], off offset:224
	v_lshl_add_u64 v[2:3], v[54:55], 0, v[50:51]
	s_mov_b64 s[18:19], 0
	v_mov_b32_e32 v4, v64
	v_mov_b32_e32 v5, v63
	global_load_dword v9, v[2:3], off
	v_lshl_add_u64 v[2:3], v[2:3], 0, s[16:17]
	global_load_dword v10, v[2:3], off
	v_lshl_add_u64 v[2:3], v[2:3], 0, s[16:17]
	global_load_dword v11, v[2:3], off
	v_lshl_add_u64 v[2:3], v[2:3], 0, s[16:17]
	global_load_dword v12, v[2:3], off
	v_lshl_add_u64 v[2:3], v[2:3], 0, s[16:17]
	global_load_dword v13, v[2:3], off
	v_lshl_add_u64 v[2:3], v[2:3], 0, s[16:17]
	global_load_dword v14, v[2:3], off
	v_lshl_add_u64 v[2:3], v[2:3], 0, s[16:17]
	global_load_dword v15, v[2:3], off
	v_lshl_add_u64 v[2:3], v[2:3], 0, s[16:17]
	global_load_dword v16, v[2:3], off
	v_lshl_add_u64 v[2:3], v[2:3], 0, s[16:17]
	global_load_dword v17, v[2:3], off
	v_lshl_add_u64 v[2:3], v[2:3], 0, s[16:17]
	global_load_dword v74, v[2:3], off
	v_lshl_add_u64 v[2:3], v[2:3], 0, s[16:17]
	global_load_dword v75, v[2:3], off
	v_lshl_add_u64 v[2:3], v[2:3], 0, s[16:17]
	global_load_dword v76, v[2:3], off
	v_lshl_add_u64 v[2:3], v[2:3], 0, s[16:17]
	global_load_dword v77, v[2:3], off
	v_lshl_add_u64 v[2:3], v[2:3], 0, s[16:17]
	global_load_dword v78, v[2:3], off
	v_lshl_add_u64 v[2:3], v[2:3], 0, s[16:17]
	global_load_dword v79, v[2:3], off
	v_lshl_add_u64 v[2:3], v[2:3], 0, s[16:17]
	global_load_dword v80, v[2:3], off
	s_waitcnt vmcnt(0)
	v_cmp_gt_i32_e32 vcc, s39, v63
	v_mad_u32_u24 v8, v63, s35, v60
	v_lshl_add_u32 v8, v8, 1, 0
	v_cndmask_b32_e32 v6, 0, v9, vcc
	v_bfe_u32 v7, v6, 16, 1
	v_add3_u32 v7, v6, v7, s34
	v_and_b32_e32 v82, 0xffff0000, v7
	v_sub_f32_e32 v6, v6, v82
	ds_write_b16_d16_hi v8, v7
	v_bfe_u32 v7, v6, 16, 1
	v_add3_u32 v6, v6, v7, s34
	ds_write_b16_d16_hi v8, v6 offset:17408
	v_add_u32_e32 v81, 4, v63
	v_cmp_gt_i32_e32 vcc, s39, v81
	v_mad_u32_u24 v8, v81, s35, v60
	v_lshl_add_u32 v8, v8, 1, 0
	v_cndmask_b32_e32 v6, 0, v10, vcc
	v_bfe_u32 v7, v6, 16, 1
	v_add3_u32 v7, v6, v7, s34
	v_and_b32_e32 v82, 0xffff0000, v7
	v_sub_f32_e32 v6, v6, v82
	ds_write_b16_d16_hi v8, v7
	v_bfe_u32 v7, v6, 16, 1
	v_add3_u32 v6, v6, v7, s34
	ds_write_b16_d16_hi v8, v6 offset:17408
	v_add_u32_e32 v81, 8, v63
	v_cmp_gt_i32_e32 vcc, s39, v81
	v_mad_u32_u24 v8, v81, s35, v60
	v_lshl_add_u32 v8, v8, 1, 0
	v_cndmask_b32_e32 v6, 0, v11, vcc
	v_bfe_u32 v7, v6, 16, 1
	v_add3_u32 v7, v6, v7, s34
	v_and_b32_e32 v82, 0xffff0000, v7
	v_sub_f32_e32 v6, v6, v82
	ds_write_b16_d16_hi v8, v7
	v_bfe_u32 v7, v6, 16, 1
	v_add3_u32 v6, v6, v7, s34
	ds_write_b16_d16_hi v8, v6 offset:17408
	v_add_u32_e32 v81, 12, v63
	v_cmp_gt_i32_e32 vcc, s39, v81
	v_mad_u32_u24 v8, v81, s35, v60
	v_lshl_add_u32 v8, v8, 1, 0
	v_cndmask_b32_e32 v6, 0, v12, vcc
	v_bfe_u32 v7, v6, 16, 1
	v_add3_u32 v7, v6, v7, s34
	v_and_b32_e32 v82, 0xffff0000, v7
	v_sub_f32_e32 v6, v6, v82
	ds_write_b16_d16_hi v8, v7
	v_bfe_u32 v7, v6, 16, 1
	v_add3_u32 v6, v6, v7, s34
	ds_write_b16_d16_hi v8, v6 offset:17408
	v_add_u32_e32 v81, 16, v63
	v_cmp_gt_i32_e32 vcc, s39, v81
	v_mad_u32_u24 v8, v81, s35, v60
	v_lshl_add_u32 v8, v8, 1, 0
	v_cndmask_b32_e32 v6, 0, v13, vcc
	v_bfe_u32 v7, v6, 16, 1
	v_add3_u32 v7, v6, v7, s34
	v_and_b32_e32 v82, 0xffff0000, v7
	v_sub_f32_e32 v6, v6, v82
	ds_write_b16_d16_hi v8, v7
	v_bfe_u32 v7, v6, 16, 1
	v_add3_u32 v6, v6, v7, s34
	ds_write_b16_d16_hi v8, v6 offset:17408
	v_add_u32_e32 v81, 20, v63
	v_cmp_gt_i32_e32 vcc, s39, v81
	v_mad_u32_u24 v8, v81, s35, v60
	v_lshl_add_u32 v8, v8, 1, 0
	v_cndmask_b32_e32 v6, 0, v14, vcc
	v_bfe_u32 v7, v6, 16, 1
	v_add3_u32 v7, v6, v7, s34
	v_and_b32_e32 v82, 0xffff0000, v7
	v_sub_f32_e32 v6, v6, v82
	ds_write_b16_d16_hi v8, v7
	v_bfe_u32 v7, v6, 16, 1
	v_add3_u32 v6, v6, v7, s34
	ds_write_b16_d16_hi v8, v6 offset:17408
	v_add_u32_e32 v81, 24, v63
	v_cmp_gt_i32_e32 vcc, s39, v81
	v_mad_u32_u24 v8, v81, s35, v60
	v_lshl_add_u32 v8, v8, 1, 0
	v_cndmask_b32_e32 v6, 0, v15, vcc
	v_bfe_u32 v7, v6, 16, 1
	v_add3_u32 v7, v6, v7, s34
	v_and_b32_e32 v82, 0xffff0000, v7
	v_sub_f32_e32 v6, v6, v82
	ds_write_b16_d16_hi v8, v7
	v_bfe_u32 v7, v6, 16, 1
	v_add3_u32 v6, v6, v7, s34
	ds_write_b16_d16_hi v8, v6 offset:17408
	v_add_u32_e32 v81, 28, v63
	v_cmp_gt_i32_e32 vcc, s39, v81
	v_mad_u32_u24 v8, v81, s35, v60
	v_lshl_add_u32 v8, v8, 1, 0
	v_cndmask_b32_e32 v6, 0, v16, vcc
	v_bfe_u32 v7, v6, 16, 1
	v_add3_u32 v7, v6, v7, s34
	v_and_b32_e32 v82, 0xffff0000, v7
	v_sub_f32_e32 v6, v6, v82
	ds_write_b16_d16_hi v8, v7
	v_bfe_u32 v7, v6, 16, 1
	v_add3_u32 v6, v6, v7, s34
	ds_write_b16_d16_hi v8, v6 offset:17408
	v_add_u32_e32 v81, 32, v63
	v_cmp_gt_i32_e32 vcc, s39, v81
	v_mad_u32_u24 v8, v81, s35, v60
	v_lshl_add_u32 v8, v8, 1, 0
	v_cndmask_b32_e32 v6, 0, v17, vcc
	v_bfe_u32 v7, v6, 16, 1
	v_add3_u32 v7, v6, v7, s34
	v_and_b32_e32 v82, 0xffff0000, v7
	v_sub_f32_e32 v6, v6, v82
	ds_write_b16_d16_hi v8, v7
	v_bfe_u32 v7, v6, 16, 1
	v_add3_u32 v6, v6, v7, s34
	ds_write_b16_d16_hi v8, v6 offset:17408
	v_add_u32_e32 v81, 36, v63
	v_cmp_gt_i32_e32 vcc, s39, v81
	v_mad_u32_u24 v8, v81, s35, v60
	v_lshl_add_u32 v8, v8, 1, 0
	v_cndmask_b32_e32 v6, 0, v74, vcc
	v_bfe_u32 v7, v6, 16, 1
	v_add3_u32 v7, v6, v7, s34
	v_and_b32_e32 v82, 0xffff0000, v7
	v_sub_f32_e32 v6, v6, v82
	ds_write_b16_d16_hi v8, v7
	v_bfe_u32 v7, v6, 16, 1
	v_add3_u32 v6, v6, v7, s34
	ds_write_b16_d16_hi v8, v6 offset:17408
	v_add_u32_e32 v81, 40, v63
	v_cmp_gt_i32_e32 vcc, s39, v81
	v_mad_u32_u24 v8, v81, s35, v60
	v_lshl_add_u32 v8, v8, 1, 0
	v_cndmask_b32_e32 v6, 0, v75, vcc
	v_bfe_u32 v7, v6, 16, 1
	v_add3_u32 v7, v6, v7, s34
	v_and_b32_e32 v82, 0xffff0000, v7
	v_sub_f32_e32 v6, v6, v82
	ds_write_b16_d16_hi v8, v7
	v_bfe_u32 v7, v6, 16, 1
	v_add3_u32 v6, v6, v7, s34
	ds_write_b16_d16_hi v8, v6 offset:17408
	v_add_u32_e32 v81, 44, v63
	v_cmp_gt_i32_e32 vcc, s39, v81
	v_mad_u32_u24 v8, v81, s35, v60
	v_lshl_add_u32 v8, v8, 1, 0
	v_cndmask_b32_e32 v6, 0, v76, vcc
	v_bfe_u32 v7, v6, 16, 1
	v_add3_u32 v7, v6, v7, s34
	v_and_b32_e32 v82, 0xffff0000, v7
	v_sub_f32_e32 v6, v6, v82
	ds_write_b16_d16_hi v8, v7
	v_bfe_u32 v7, v6, 16, 1
	v_add3_u32 v6, v6, v7, s34
	ds_write_b16_d16_hi v8, v6 offset:17408
	v_add_u32_e32 v81, 48, v63
	v_cmp_gt_i32_e32 vcc, s39, v81
	v_mad_u32_u24 v8, v81, s35, v60
	v_lshl_add_u32 v8, v8, 1, 0
	v_cndmask_b32_e32 v6, 0, v77, vcc
	v_bfe_u32 v7, v6, 16, 1
	v_add3_u32 v7, v6, v7, s34
	v_and_b32_e32 v82, 0xffff0000, v7
	v_sub_f32_e32 v6, v6, v82
	ds_write_b16_d16_hi v8, v7
	v_bfe_u32 v7, v6, 16, 1
	v_add3_u32 v6, v6, v7, s34
	ds_write_b16_d16_hi v8, v6 offset:17408
	v_add_u32_e32 v81, 52, v63
	v_cmp_gt_i32_e32 vcc, s39, v81
	v_mad_u32_u24 v8, v81, s35, v60
	v_lshl_add_u32 v8, v8, 1, 0
	v_cndmask_b32_e32 v6, 0, v78, vcc
	v_bfe_u32 v7, v6, 16, 1
	v_add3_u32 v7, v6, v7, s34
	v_and_b32_e32 v82, 0xffff0000, v7
	v_sub_f32_e32 v6, v6, v82
	ds_write_b16_d16_hi v8, v7
	v_bfe_u32 v7, v6, 16, 1
	v_add3_u32 v6, v6, v7, s34
	ds_write_b16_d16_hi v8, v6 offset:17408
	v_add_u32_e32 v81, 56, v63
	v_cmp_gt_i32_e32 vcc, s39, v81
	v_mad_u32_u24 v8, v81, s35, v60
	v_lshl_add_u32 v8, v8, 1, 0
	v_cndmask_b32_e32 v6, 0, v79, vcc
	v_bfe_u32 v7, v6, 16, 1
	v_add3_u32 v7, v6, v7, s34
	v_and_b32_e32 v82, 0xffff0000, v7
	v_sub_f32_e32 v6, v6, v82
	ds_write_b16_d16_hi v8, v7
	v_bfe_u32 v7, v6, 16, 1
	v_add3_u32 v6, v6, v7, s34
	ds_write_b16_d16_hi v8, v6 offset:17408
	v_add_u32_e32 v81, 60, v63
	v_cmp_gt_i32_e32 vcc, s39, v81
	v_mad_u32_u24 v8, v81, s35, v60
	v_lshl_add_u32 v8, v8, 1, 0
	v_cndmask_b32_e32 v6, 0, v80, vcc
	v_bfe_u32 v7, v6, 16, 1
	v_add3_u32 v7, v6, v7, s34
	v_and_b32_e32 v82, 0xffff0000, v7
	v_sub_f32_e32 v6, v6, v82
	ds_write_b16_d16_hi v8, v7
	v_bfe_u32 v7, v6, 16, 1
	v_add3_u32 v6, v6, v7, s34
	ds_write_b16_d16_hi v8, v6 offset:17408
